# P7 routing: top-16 of 64 scores by a sorting network (4 x sort16 + bitonic top-k merges) instead of 64 serial insertions; all 64 scores read from LDS in one batch
# speedup vs baseline: 1.0470x; 1.0082x over previous
; DI void routing_block(LAS unsigned char* lds, const bf16* q, const bf16* skb, int* experts, float* pgates, int tb) {
;     ...
;         const int t0 = tb * 32, hc = 8 * hp + wave;
;         f32x16 acc[4];
; #pragma unroll
;         for (int kb = 0; kb < 4; ++kb)
; #pragma unroll
;             for (int i = 0; i < 16; ++i) acc[kb][i] = 0.f;
; #pragma unroll
;         for (int ks = 0; ks < 8; ++ks) {
;             const bf16x8 a = *(const bf16x8*)(q + (size_t)(t0 + r) * QW + hc * 128 + 16 * ks + 8 * h);
; #pragma unroll
;             for (int kb = 0; kb < 4; ++kb) {
;                 const bf16x8 b = *(const bf16x8*)(skb + ((size_t)hc * 128 + 32 * kb + r) * 128 + 16 * ks + 8 * h);
;                 acc[kb] = __builtin_amdgcn_mfma_f32_32x32x16_bf16(a, b, acc[kb], 0, 0, 0);
;             }
;         }
.LBB0_894:
	s_lshl_b32 s76, s78, 3
	s_add_i32 s76, s76, s79
	s_lshl_b32 vcc_lo, s76, 7
	s_ashr_i32 vcc_hi, vcc_lo, 31
	v_lshl_add_u64 v[110:111], vcc, 1, v[80:81]
	s_ashr_i32 s77, s76, 31
	global_load_dwordx4 v[146:149], v[110:111], off
	global_load_dwordx4 v[150:153], v[110:111], off offset:32
	global_load_dwordx4 v[154:157], v[110:111], off offset:64
	global_load_dwordx4 v[158:161], v[110:111], off offset:96
	global_load_dwordx4 v[162:165], v[110:111], off offset:128
	global_load_dwordx4 v[166:169], v[110:111], off offset:160
	global_load_dwordx4 v[170:173], v[110:111], off offset:192
	global_load_dwordx4 v[174:177], v[110:111], off offset:224
	s_lshl_b64 s[76:77], s[76:77], 15
	v_mov_b32_e32 v105, s77
	v_or_b32_e32 v104, s76, v102
	v_lshl_add_u64 v[112:113], v[82:83], 0, v[104:105]
	v_or_b32_e32 v108, 0x2000, v104
	v_mov_b32_e32 v109, s77
	v_or_b32_e32 v106, 0x4000, v104
	v_mov_b32_e32 v107, s77
	v_or_b32_e32 v104, 0x6000, v104
	v_lshl_add_u64 v[242:243], v[82:83], 0, v[108:109]
	v_lshl_add_u64 v[244:245], v[82:83], 0, v[106:107]
	v_lshl_add_u64 v[246:247], v[82:83], 0, v[104:105]
	global_load_dwordx4 v[178:181], v[112:113], off
	global_load_dwordx4 v[182:185], v[242:243], off
	global_load_dwordx4 v[186:189], v[244:245], off
	global_load_dwordx4 v[190:193], v[246:247], off
	global_load_dwordx4 v[194:197], v[112:113], off offset:32
	global_load_dwordx4 v[198:201], v[242:243], off offset:32
	global_load_dwordx4 v[202:205], v[244:245], off offset:32
	global_load_dwordx4 v[206:209], v[246:247], off offset:32
	global_load_dwordx4 v[210:213], v[112:113], off offset:64
	global_load_dwordx4 v[214:217], v[242:243], off offset:64
	global_load_dwordx4 v[218:221], v[244:245], off offset:64
	global_load_dwordx4 v[222:225], v[246:247], off offset:64
	global_load_dwordx4 v[226:229], v[112:113], off offset:96
	global_load_dwordx4 v[230:233], v[242:243], off offset:96
	global_load_dwordx4 v[234:237], v[244:245], off offset:96
	global_load_dwordx4 v[238:241], v[246:247], off offset:96
	s_xor_b64 s[74:75], s[74:75], -1
	s_mov_b32 s76, 0
	s_waitcnt vmcnt(12)
	v_mfma_f32_32x32x16_bf16 v[50:65], v[146:149], v[178:181], 0
	v_mfma_f32_32x32x16_bf16 v[34:49], v[146:149], v[182:185], 0
	v_mfma_f32_32x32x16_bf16 v[18:33], v[146:149], v[186:189], 0
	v_mfma_f32_32x32x16_bf16 v[2:17], v[146:149], v[190:193], 0
	global_load_dwordx4 v[178:181], v[112:113], off offset:128
	global_load_dwordx4 v[182:185], v[242:243], off offset:128
	global_load_dwordx4 v[186:189], v[244:245], off offset:128
	global_load_dwordx4 v[190:193], v[246:247], off offset:128
	s_waitcnt vmcnt(12)
	v_mfma_f32_32x32x16_bf16 v[50:65], v[150:153], v[194:197], v[50:65]
	v_mfma_f32_32x32x16_bf16 v[34:49], v[150:153], v[198:201], v[34:49]
	v_mfma_f32_32x32x16_bf16 v[18:33], v[150:153], v[202:205], v[18:33]
	v_mfma_f32_32x32x16_bf16 v[2:17], v[150:153], v[206:209], v[2:17]
	global_load_dwordx4 v[194:197], v[112:113], off offset:160
	global_load_dwordx4 v[198:201], v[242:243], off offset:160
	global_load_dwordx4 v[202:205], v[244:245], off offset:160
	global_load_dwordx4 v[206:209], v[246:247], off offset:160
	s_waitcnt vmcnt(12)
	v_mfma_f32_32x32x16_bf16 v[50:65], v[154:157], v[210:213], v[50:65]
	v_mfma_f32_32x32x16_bf16 v[34:49], v[154:157], v[214:217], v[34:49]
	v_mfma_f32_32x32x16_bf16 v[18:33], v[154:157], v[218:221], v[18:33]
	v_mfma_f32_32x32x16_bf16 v[2:17], v[154:157], v[222:225], v[2:17]
	global_load_dwordx4 v[210:213], v[112:113], off offset:192
	global_load_dwordx4 v[214:217], v[242:243], off offset:192
	global_load_dwordx4 v[218:221], v[244:245], off offset:192
	global_load_dwordx4 v[222:225], v[246:247], off offset:192
	s_waitcnt vmcnt(12)
	v_mfma_f32_32x32x16_bf16 v[50:65], v[158:161], v[226:229], v[50:65]
	v_mfma_f32_32x32x16_bf16 v[34:49], v[158:161], v[230:233], v[34:49]
	v_mfma_f32_32x32x16_bf16 v[18:33], v[158:161], v[234:237], v[18:33]
	v_mfma_f32_32x32x16_bf16 v[2:17], v[158:161], v[238:241], v[2:17]
	global_load_dwordx4 v[226:229], v[112:113], off offset:224
	global_load_dwordx4 v[230:233], v[242:243], off offset:224
	global_load_dwordx4 v[234:237], v[244:245], off offset:224
	global_load_dwordx4 v[238:241], v[246:247], off offset:224
	s_waitcnt vmcnt(12)
	v_mfma_f32_32x32x16_bf16 v[50:65], v[162:165], v[178:181], v[50:65]
	v_mfma_f32_32x32x16_bf16 v[34:49], v[162:165], v[182:185], v[34:49]
	v_mfma_f32_32x32x16_bf16 v[18:33], v[162:165], v[186:189], v[18:33]
	v_mfma_f32_32x32x16_bf16 v[2:17], v[162:165], v[190:193], v[2:17]
	s_waitcnt vmcnt(8)
	v_mfma_f32_32x32x16_bf16 v[50:65], v[166:169], v[194:197], v[50:65]
	v_mfma_f32_32x32x16_bf16 v[34:49], v[166:169], v[198:201], v[34:49]
	v_mfma_f32_32x32x16_bf16 v[18:33], v[166:169], v[202:205], v[18:33]
	v_mfma_f32_32x32x16_bf16 v[2:17], v[166:169], v[206:209], v[2:17]
	s_waitcnt vmcnt(4)
	v_mfma_f32_32x32x16_bf16 v[50:65], v[170:173], v[210:213], v[50:65]
	v_mfma_f32_32x32x16_bf16 v[34:49], v[170:173], v[214:217], v[34:49]
	v_mfma_f32_32x32x16_bf16 v[18:33], v[170:173], v[218:221], v[18:33]
	v_mfma_f32_32x32x16_bf16 v[2:17], v[170:173], v[222:225], v[2:17]
	s_waitcnt vmcnt(0)
; DI int crow(int reg, int h) { return (reg & 3) + 8 * (reg >> 2) + 4 * h; }
; DI void routing_block(LAS unsigned char* lds, const bf16* q, const bf16* skb, int* experts, float* pgates, int tb) {
;     ...
; #pragma unroll
;         for (int kb = 0; kb < 4; ++kb)
; #pragma unroll
;             for (int i = 0; i < 16; ++i) {
;                 const int key = 32 * kb + r;
;                 sc[(crow(i, h) * 8 + wave) * RT_PITCH + key] = (f2key(acc[kb][i]) & ~127) | key;
;             }
	v_mfma_f32_32x32x16_bf16 v[50:65], v[174:177], v[226:229], v[50:65]
	v_mfma_f32_32x32x16_bf16 v[34:49], v[174:177], v[230:233], v[34:49]
	v_mfma_f32_32x32x16_bf16 v[18:33], v[174:177], v[234:237], v[18:33]
	v_mfma_f32_32x32x16_bf16 v[2:17], v[174:177], v[238:241], v[2:17]
	s_nop 11
	v_ashrrev_i32_e32 v105, 31, v51
	v_and_b32_e32 v105, 0x7fffff80, v105
	v_and_b32_e32 v51, 0xffffff80, v51
	v_bitop3_b32 v51, v105, v103, v51 bitop3:0xde
	v_ashrrev_i32_e32 v105, 31, v52
	v_and_b32_e32 v105, 0x7fffff80, v105
	v_and_b32_e32 v52, 0xffffff80, v52
	v_bitop3_b32 v52, v105, v103, v52 bitop3:0xde
	v_ashrrev_i32_e32 v105, 31, v53
	v_and_b32_e32 v105, 0x7fffff80, v105
	v_and_b32_e32 v53, 0xffffff80, v53
	v_bitop3_b32 v53, v105, v103, v53 bitop3:0xde
	v_ashrrev_i32_e32 v105, 31, v54
	v_and_b32_e32 v105, 0x7fffff80, v105
	v_and_b32_e32 v54, 0xffffff80, v54
	v_bitop3_b32 v54, v105, v103, v54 bitop3:0xde
	v_ashrrev_i32_e32 v105, 31, v55
	v_and_b32_e32 v105, 0x7fffff80, v105
	v_and_b32_e32 v55, 0xffffff80, v55
	v_bitop3_b32 v55, v105, v103, v55 bitop3:0xde
	v_ashrrev_i32_e32 v105, 31, v56
	v_and_b32_e32 v105, 0x7fffff80, v105
	v_and_b32_e32 v56, 0xffffff80, v56
	v_bitop3_b32 v56, v105, v103, v56 bitop3:0xde
	v_ashrrev_i32_e32 v105, 31, v57
	v_and_b32_e32 v105, 0x7fffff80, v105
	v_and_b32_e32 v57, 0xffffff80, v57
	v_bitop3_b32 v57, v105, v103, v57 bitop3:0xde
	v_ashrrev_i32_e32 v105, 31, v58
	v_and_b32_e32 v105, 0x7fffff80, v105
	v_and_b32_e32 v58, 0xffffff80, v58
	v_bitop3_b32 v58, v105, v103, v58 bitop3:0xde
	v_ashrrev_i32_e32 v105, 31, v59
	v_and_b32_e32 v105, 0x7fffff80, v105
	v_and_b32_e32 v59, 0xffffff80, v59
	v_bitop3_b32 v59, v105, v103, v59 bitop3:0xde
	v_ashrrev_i32_e32 v105, 31, v60
	v_and_b32_e32 v105, 0x7fffff80, v105
	v_and_b32_e32 v60, 0xffffff80, v60
	v_bitop3_b32 v60, v105, v103, v60 bitop3:0xde
	v_ashrrev_i32_e32 v105, 31, v61
	v_and_b32_e32 v105, 0x7fffff80, v105
	v_and_b32_e32 v61, 0xffffff80, v61
	v_bitop3_b32 v61, v105, v103, v61 bitop3:0xde
	v_ashrrev_i32_e32 v105, 31, v62
	v_and_b32_e32 v105, 0x7fffff80, v105
	v_and_b32_e32 v62, 0xffffff80, v62
	v_bitop3_b32 v62, v105, v103, v62 bitop3:0xde
	v_ashrrev_i32_e32 v105, 31, v63
	v_and_b32_e32 v105, 0x7fffff80, v105
	v_and_b32_e32 v63, 0xffffff80, v63
	v_bitop3_b32 v63, v105, v103, v63 bitop3:0xde
	v_ashrrev_i32_e32 v105, 31, v64
	v_and_b32_e32 v105, 0x7fffff80, v105
	v_and_b32_e32 v64, 0xffffff80, v64
	v_bitop3_b32 v64, v105, v103, v64 bitop3:0xde
	v_ashrrev_i32_e32 v105, 31, v65
	v_and_b32_e32 v105, 0x7fffff80, v105
	v_and_b32_e32 v65, 0xffffff80, v65
	v_ashrrev_i32_e32 v104, 31, v50
	v_bitop3_b32 v65, v105, v103, v65 bitop3:0xde
	v_ashrrev_i32_e32 v105, 31, v34
	v_and_b32_e32 v104, 0x7fffff80, v104
	v_and_b32_e32 v50, 0xffffff80, v50
	v_and_b32_e32 v105, 0x7fffff80, v105
	v_and_b32_e32 v34, 0xffffff80, v34
	v_bitop3_b32 v50, v104, v103, v50 bitop3:0xde
	v_add_u32_e32 v104, v123, v124
	v_bitop3_b32 v34, v105, v125, v34 bitop3:0xde
	ds_write2_b32 v104, v50, v34 offset1:32
	v_ashrrev_i32_e32 v34, 31, v35
	v_and_b32_e32 v34, 0x7fffff80, v34
	v_and_b32_e32 v35, 0xffffff80, v35
	v_bitop3_b32 v34, v34, v125, v35 bitop3:0xde
	v_add_u32_e32 v35, 0x1000, v104
	ds_write2_b32 v35, v51, v34 offset0:8 offset1:40
	v_ashrrev_i32_e32 v34, 31, v36
	v_and_b32_e32 v34, 0x7fffff80, v34
	v_and_b32_e32 v36, 0xffffff80, v36
	v_bitop3_b32 v34, v34, v125, v36 bitop3:0xde
	v_add_u32_e32 v36, 0x2000, v104
	ds_write2_b32 v36, v52, v34 offset0:16 offset1:48
	v_ashrrev_i32_e32 v34, 31, v37
	v_and_b32_e32 v34, 0x7fffff80, v34
	v_and_b32_e32 v37, 0xffffff80, v37
	v_bitop3_b32 v34, v34, v125, v37 bitop3:0xde
	v_add_u32_e32 v37, 0x3000, v104
	ds_write2_b32 v37, v53, v34 offset0:24 offset1:56
	v_ashrrev_i32_e32 v34, 31, v38
	v_and_b32_e32 v34, 0x7fffff80, v34
	v_and_b32_e32 v38, 0xffffff80, v38
	v_bitop3_b32 v34, v34, v125, v38 bitop3:0xde
	v_add_u32_e32 v38, 0x8000, v104
	ds_write2_b32 v38, v54, v34 offset0:64 offset1:96
	v_ashrrev_i32_e32 v34, 31, v39
	v_and_b32_e32 v34, 0x7fffff80, v34
	v_and_b32_e32 v39, 0xffffff80, v39
	v_bitop3_b32 v34, v34, v125, v39 bitop3:0xde
	v_add_u32_e32 v39, 0x9000, v104
	ds_write2_b32 v39, v55, v34 offset0:72 offset1:104
	v_ashrrev_i32_e32 v34, 31, v40
	v_and_b32_e32 v34, 0x7fffff80, v34
	v_and_b32_e32 v40, 0xffffff80, v40
	v_bitop3_b32 v34, v34, v125, v40 bitop3:0xde
	v_add_u32_e32 v40, 0xa000, v104
	ds_write2_b32 v40, v56, v34 offset0:80 offset1:112
	v_ashrrev_i32_e32 v34, 31, v41
	v_and_b32_e32 v34, 0x7fffff80, v34
	v_and_b32_e32 v41, 0xffffff80, v41
	v_bitop3_b32 v34, v34, v125, v41 bitop3:0xde
	v_add_u32_e32 v41, 0xb000, v104
	ds_write2_b32 v41, v57, v34 offset0:88 offset1:120
	v_ashrrev_i32_e32 v34, 31, v42
	v_and_b32_e32 v34, 0x7fffff80, v34
	v_and_b32_e32 v42, 0xffffff80, v42
	v_bitop3_b32 v34, v34, v125, v42 bitop3:0xde
	ds_write2_b32 v128, v58, v34 offset1:32
	v_ashrrev_i32_e32 v34, 31, v43
	v_and_b32_e32 v34, 0x7fffff80, v34
	v_and_b32_e32 v42, 0xffffff80, v43
	v_bitop3_b32 v34, v34, v125, v42 bitop3:0xde
	ds_write2_b32 v129, v59, v34 offset1:32
	v_ashrrev_i32_e32 v34, 31, v44
	v_and_b32_e32 v34, 0x7fffff80, v34
	v_and_b32_e32 v42, 0xffffff80, v44
	v_bitop3_b32 v34, v34, v125, v42 bitop3:0xde
	ds_write2_b32 v130, v60, v34 offset1:32
	v_ashrrev_i32_e32 v34, 31, v45
	v_and_b32_e32 v34, 0x7fffff80, v34
	v_and_b32_e32 v42, 0xffffff80, v45
	v_bitop3_b32 v34, v34, v125, v42 bitop3:0xde
	ds_write2_b32 v131, v61, v34 offset1:32
	v_ashrrev_i32_e32 v34, 31, v46
	v_and_b32_e32 v34, 0x7fffff80, v34
	v_and_b32_e32 v42, 0xffffff80, v46
	v_bitop3_b32 v34, v34, v125, v42 bitop3:0xde
	ds_write2_b32 v132, v62, v34 offset1:32
	v_ashrrev_i32_e32 v34, 31, v47
	v_and_b32_e32 v34, 0x7fffff80, v34
; DI int crow(int reg, int h) { return (reg & 3) + 8 * (reg >> 2) + 4 * h; }
; DI void routing_block(LAS unsigned char* lds, const bf16* q, const bf16* skb, int* experts, float* pgates, int tb) {
;     ...
; #pragma unroll
;         for (int kb = 0; kb < 4; ++kb)
; #pragma unroll
;             for (int i = 0; i < 16; ++i) {
;                 const int key = 32 * kb + r;
;                 sc[(crow(i, h) * 8 + wave) * RT_PITCH + key] = (f2key(acc[kb][i]) & ~127) | key;
;             }
;         __syncthreads();
;         {
;             int a[16];
; #pragma unroll
;             for (int j = 0; j < 16; ++j) a[j] = (int)0x80000000;
	v_and_b32_e32 v42, 0xffffff80, v47
	v_bitop3_b32 v34, v34, v125, v42 bitop3:0xde
	ds_write2_b32 v133, v63, v34 offset1:32
	v_ashrrev_i32_e32 v34, 31, v48
	v_and_b32_e32 v34, 0x7fffff80, v34
	v_and_b32_e32 v42, 0xffffff80, v48
	v_bitop3_b32 v34, v34, v125, v42 bitop3:0xde
	ds_write2_b32 v134, v64, v34 offset1:32
	v_ashrrev_i32_e32 v34, 31, v49
	v_and_b32_e32 v34, 0x7fffff80, v34
	v_and_b32_e32 v42, 0xffffff80, v49
	v_bitop3_b32 v34, v34, v125, v42 bitop3:0xde
	ds_write2_b32 v135, v65, v34 offset1:32
	v_ashrrev_i32_e32 v34, 31, v18
	v_and_b32_e32 v34, 0x7fffff80, v34
	v_and_b32_e32 v18, 0xffffff80, v18
	v_bitop3_b32 v18, v34, v126, v18 bitop3:0xde
	v_ashrrev_i32_e32 v34, 31, v19
	v_and_b32_e32 v34, 0x7fffff80, v34
	v_and_b32_e32 v19, 0xffffff80, v19
	v_bitop3_b32 v19, v34, v126, v19 bitop3:0xde
	v_ashrrev_i32_e32 v34, 31, v20
	v_and_b32_e32 v34, 0x7fffff80, v34
	v_and_b32_e32 v20, 0xffffff80, v20
	v_bitop3_b32 v20, v34, v126, v20 bitop3:0xde
	v_ashrrev_i32_e32 v34, 31, v21
	v_and_b32_e32 v34, 0x7fffff80, v34
	v_and_b32_e32 v21, 0xffffff80, v21
	v_bitop3_b32 v21, v34, v126, v21 bitop3:0xde
	v_ashrrev_i32_e32 v34, 31, v22
	v_and_b32_e32 v34, 0x7fffff80, v34
	v_and_b32_e32 v22, 0xffffff80, v22
	v_bitop3_b32 v22, v34, v126, v22 bitop3:0xde
	v_ashrrev_i32_e32 v34, 31, v23
	v_and_b32_e32 v34, 0x7fffff80, v34
	v_and_b32_e32 v23, 0xffffff80, v23
	v_bitop3_b32 v23, v34, v126, v23 bitop3:0xde
	v_ashrrev_i32_e32 v34, 31, v24
	v_and_b32_e32 v34, 0x7fffff80, v34
	v_and_b32_e32 v24, 0xffffff80, v24
	v_bitop3_b32 v24, v34, v126, v24 bitop3:0xde
	v_ashrrev_i32_e32 v34, 31, v25
	v_and_b32_e32 v34, 0x7fffff80, v34
	v_and_b32_e32 v25, 0xffffff80, v25
	v_bitop3_b32 v25, v34, v126, v25 bitop3:0xde
	v_ashrrev_i32_e32 v34, 31, v26
	v_and_b32_e32 v34, 0x7fffff80, v34
	v_and_b32_e32 v26, 0xffffff80, v26
	v_bitop3_b32 v26, v34, v126, v26 bitop3:0xde
	v_ashrrev_i32_e32 v34, 31, v27
	v_and_b32_e32 v34, 0x7fffff80, v34
	v_and_b32_e32 v27, 0xffffff80, v27
	v_bitop3_b32 v27, v34, v126, v27 bitop3:0xde
	v_ashrrev_i32_e32 v34, 31, v28
	v_and_b32_e32 v34, 0x7fffff80, v34
	v_and_b32_e32 v28, 0xffffff80, v28
	v_bitop3_b32 v28, v34, v126, v28 bitop3:0xde
	v_ashrrev_i32_e32 v34, 31, v29
	v_and_b32_e32 v34, 0x7fffff80, v34
	v_and_b32_e32 v29, 0xffffff80, v29
	v_bitop3_b32 v29, v34, v126, v29 bitop3:0xde
	v_ashrrev_i32_e32 v34, 31, v30
	v_and_b32_e32 v34, 0x7fffff80, v34
	v_and_b32_e32 v30, 0xffffff80, v30
	v_bitop3_b32 v30, v34, v126, v30 bitop3:0xde
	v_ashrrev_i32_e32 v34, 31, v31
	v_and_b32_e32 v34, 0x7fffff80, v34
	v_and_b32_e32 v31, 0xffffff80, v31
	v_bitop3_b32 v31, v34, v126, v31 bitop3:0xde
	v_ashrrev_i32_e32 v34, 31, v32
	v_and_b32_e32 v34, 0x7fffff80, v34
	v_and_b32_e32 v32, 0xffffff80, v32
	v_bitop3_b32 v32, v34, v126, v32 bitop3:0xde
	v_ashrrev_i32_e32 v34, 31, v33
	v_and_b32_e32 v34, 0x7fffff80, v34
	v_and_b32_e32 v33, 0xffffff80, v33
	v_bitop3_b32 v33, v34, v126, v33 bitop3:0xde
	v_ashrrev_i32_e32 v34, 31, v2
	v_and_b32_e32 v34, 0x7fffff80, v34
	v_and_b32_e32 v2, 0xffffff80, v2
	v_bitop3_b32 v2, v34, v127, v2 bitop3:0xde
	ds_write2_b32 v104, v18, v2 offset0:64 offset1:96
	v_ashrrev_i32_e32 v2, 31, v3
	v_and_b32_e32 v2, 0x7fffff80, v2
	v_and_b32_e32 v3, 0xffffff80, v3
	v_bitop3_b32 v2, v2, v127, v3 bitop3:0xde
	ds_write2_b32 v35, v19, v2 offset0:72 offset1:104
	v_ashrrev_i32_e32 v2, 31, v4
	v_and_b32_e32 v2, 0x7fffff80, v2
	v_and_b32_e32 v3, 0xffffff80, v4
	v_bitop3_b32 v2, v2, v127, v3 bitop3:0xde
	ds_write2_b32 v36, v20, v2 offset0:80 offset1:112
	v_ashrrev_i32_e32 v2, 31, v5
	v_and_b32_e32 v2, 0x7fffff80, v2
	v_and_b32_e32 v3, 0xffffff80, v5
	v_bitop3_b32 v2, v2, v127, v3 bitop3:0xde
	ds_write2_b32 v37, v21, v2 offset0:88 offset1:120
	v_ashrrev_i32_e32 v2, 31, v6
	v_and_b32_e32 v2, 0x7fffff80, v2
	v_and_b32_e32 v3, 0xffffff80, v6
	v_bitop3_b32 v2, v2, v127, v3 bitop3:0xde
	ds_write2_b32 v38, v22, v2 offset0:128 offset1:160
	v_ashrrev_i32_e32 v2, 31, v7
	v_and_b32_e32 v2, 0x7fffff80, v2
	v_and_b32_e32 v3, 0xffffff80, v7
	v_bitop3_b32 v2, v2, v127, v3 bitop3:0xde
	ds_write2_b32 v39, v23, v2 offset0:136 offset1:168
	v_ashrrev_i32_e32 v2, 31, v8
	v_and_b32_e32 v2, 0x7fffff80, v2
	v_and_b32_e32 v3, 0xffffff80, v8
	v_bitop3_b32 v2, v2, v127, v3 bitop3:0xde
	ds_write2_b32 v40, v24, v2 offset0:144 offset1:176
	v_ashrrev_i32_e32 v2, 31, v9
	v_and_b32_e32 v2, 0x7fffff80, v2
	v_and_b32_e32 v3, 0xffffff80, v9
	v_bitop3_b32 v2, v2, v127, v3 bitop3:0xde
	ds_write2_b32 v41, v25, v2 offset0:152 offset1:184
	v_ashrrev_i32_e32 v2, 31, v10
	v_and_b32_e32 v2, 0x7fffff80, v2
	v_and_b32_e32 v3, 0xffffff80, v10
	v_bitop3_b32 v2, v2, v127, v3 bitop3:0xde
	ds_write2_b32 v128, v26, v2 offset0:64 offset1:96
	v_ashrrev_i32_e32 v2, 31, v11
	v_and_b32_e32 v2, 0x7fffff80, v2
	v_and_b32_e32 v3, 0xffffff80, v11
	v_bitop3_b32 v2, v2, v127, v3 bitop3:0xde
	ds_write2_b32 v129, v27, v2 offset0:64 offset1:96
	v_ashrrev_i32_e32 v2, 31, v12
	v_and_b32_e32 v2, 0x7fffff80, v2
	v_and_b32_e32 v3, 0xffffff80, v12
	v_bitop3_b32 v2, v2, v127, v3 bitop3:0xde
	ds_write2_b32 v130, v28, v2 offset0:64 offset1:96
	v_ashrrev_i32_e32 v2, 31, v13
	v_and_b32_e32 v2, 0x7fffff80, v2
	v_and_b32_e32 v3, 0xffffff80, v13
	v_bitop3_b32 v2, v2, v127, v3 bitop3:0xde
	ds_write2_b32 v131, v29, v2 offset0:64 offset1:96
	v_ashrrev_i32_e32 v2, 31, v14
	v_and_b32_e32 v2, 0x7fffff80, v2
	v_and_b32_e32 v3, 0xffffff80, v14
	v_bitop3_b32 v2, v2, v127, v3 bitop3:0xde
	ds_write2_b32 v132, v30, v2 offset0:64 offset1:96
	v_ashrrev_i32_e32 v2, 31, v15
	v_and_b32_e32 v2, 0x7fffff80, v2
	v_and_b32_e32 v3, 0xffffff80, v15
	v_bitop3_b32 v2, v2, v127, v3 bitop3:0xde
	ds_write2_b32 v133, v31, v2 offset0:64 offset1:96
	v_ashrrev_i32_e32 v2, 31, v16
	v_and_b32_e32 v2, 0x7fffff80, v2
	v_and_b32_e32 v3, 0xffffff80, v16
	v_bitop3_b32 v2, v2, v127, v3 bitop3:0xde
	ds_write2_b32 v134, v32, v2 offset0:64 offset1:96
	v_ashrrev_i32_e32 v2, 31, v17
	v_and_b32_e32 v2, 0x7fffff80, v2
	v_and_b32_e32 v3, 0xffffff80, v17
	v_bitop3_b32 v2, v2, v127, v3 bitop3:0xde
	ds_write2_b32 v135, v33, v2 offset0:64 offset1:96
	s_waitcnt lgkmcnt(0)
	s_barrier
; #define LAS __attribute__((address_space(3)))
; #define TOPK_INSERT(arr, xx) do { int _x = (xx); _Pragma("unroll") for (int _j = 0; _j < 16; ++_j) { const int _hi = max(arr[_j], _x); _x = min(arr[_j], _x); arr[_j] = _hi; } } while (0)
; DI void routing_block(LAS unsigned char* lds, const bf16* q, const bf16* skb, int* experts, float* pgates, int tb) {
;     ...
;             int a[16];
; #pragma unroll
;             for (int j = 0; j < 16; ++j) a[j] = (int)0x80000000;
;             LAS int* row = sc + (tid >> 1) * RT_PITCH; const int hf = tid & 1;
; #pragma unroll 8
;             for (int k = 0; k < 64; ++k) { const int x = row[64 * hf + k]; TOPK_INSERT(a, x); }
	ds_read2_b32 v[146:147], v120 offset0:0 offset1:1
	ds_read2_b32 v[148:149], v120 offset0:2 offset1:3
	ds_read2_b32 v[150:151], v120 offset0:4 offset1:5
	ds_read2_b32 v[152:153], v120 offset0:6 offset1:7
	ds_read2_b32 v[154:155], v120 offset0:8 offset1:9
	ds_read2_b32 v[156:157], v120 offset0:10 offset1:11
	ds_read2_b32 v[158:159], v120 offset0:12 offset1:13
	ds_read2_b32 v[160:161], v120 offset0:14 offset1:15
	ds_read2_b32 v[162:163], v120 offset0:16 offset1:17
	ds_read2_b32 v[164:165], v120 offset0:18 offset1:19
	ds_read2_b32 v[166:167], v120 offset0:20 offset1:21
	ds_read2_b32 v[168:169], v120 offset0:22 offset1:23
	ds_read2_b32 v[170:171], v120 offset0:24 offset1:25
	ds_read2_b32 v[172:173], v120 offset0:26 offset1:27
	ds_read2_b32 v[174:175], v120 offset0:28 offset1:29
	ds_read2_b32 v[176:177], v120 offset0:30 offset1:31
	ds_read2_b32 v[178:179], v120 offset0:32 offset1:33
	ds_read2_b32 v[180:181], v120 offset0:34 offset1:35
	ds_read2_b32 v[182:183], v120 offset0:36 offset1:37
	ds_read2_b32 v[184:185], v120 offset0:38 offset1:39
	ds_read2_b32 v[186:187], v120 offset0:40 offset1:41
	ds_read2_b32 v[188:189], v120 offset0:42 offset1:43
	ds_read2_b32 v[190:191], v120 offset0:44 offset1:45
	ds_read2_b32 v[192:193], v120 offset0:46 offset1:47
	ds_read2_b32 v[194:195], v120 offset0:48 offset1:49
	ds_read2_b32 v[196:197], v120 offset0:50 offset1:51
	ds_read2_b32 v[198:199], v120 offset0:52 offset1:53
	ds_read2_b32 v[200:201], v120 offset0:54 offset1:55
	ds_read2_b32 v[202:203], v120 offset0:56 offset1:57
	ds_read2_b32 v[204:205], v120 offset0:58 offset1:59
	ds_read2_b32 v[206:207], v120 offset0:60 offset1:61
	ds_read2_b32 v[208:209], v120 offset0:62 offset1:63
	s_waitcnt lgkmcnt(0)
	v_max_i32_e32 v18, v146, v147
	v_min_i32_e32 v147, v146, v147
	v_max_i32_e32 v19, v148, v149
	v_min_i32_e32 v149, v148, v149
	v_max_i32_e32 v20, v18, v19
	v_min_i32_e32 v19, v18, v19
	v_max_i32_e32 v21, v147, v149
	v_min_i32_e32 v149, v147, v149
	v_max_i32_e32 v146, v21, v19
	v_min_i32_e32 v19, v21, v19
	v_max_i32_e32 v148, v150, v151
	v_min_i32_e32 v151, v150, v151
	v_max_i32_e32 v18, v152, v153
	v_min_i32_e32 v153, v152, v153
	v_max_i32_e32 v147, v148, v18
	v_min_i32_e32 v18, v148, v18
	v_max_i32_e32 v21, v151, v153
	v_min_i32_e32 v153, v151, v153
	v_max_i32_e32 v150, v21, v18
	v_min_i32_e32 v18, v21, v18
	v_max_i32_e32 v152, v20, v147
	v_min_i32_e32 v147, v20, v147
	v_max_i32_e32 v148, v19, v18
	v_min_i32_e32 v18, v19, v18
	v_max_i32_e32 v151, v148, v147
	v_min_i32_e32 v147, v148, v147
	v_max_i32_e32 v21, v146, v150
	v_min_i32_e32 v150, v146, v150
	v_max_i32_e32 v20, v149, v153
	v_min_i32_e32 v153, v149, v153
	v_max_i32_e32 v19, v20, v150
	v_min_i32_e32 v150, v20, v150
	v_max_i32_e32 v148, v21, v151
	v_min_i32_e32 v151, v21, v151
	v_max_i32_e32 v146, v19, v147
	v_min_i32_e32 v147, v19, v147
	v_max_i32_e32 v149, v150, v18
	v_min_i32_e32 v18, v150, v18
	v_max_i32_e32 v20, v154, v155
	v_min_i32_e32 v155, v154, v155
	v_max_i32_e32 v21, v156, v157
	v_min_i32_e32 v157, v156, v157
	v_max_i32_e32 v19, v20, v21
	v_min_i32_e32 v21, v20, v21
	v_max_i32_e32 v150, v155, v157
	v_min_i32_e32 v157, v155, v157
	v_max_i32_e32 v154, v150, v21
	v_min_i32_e32 v21, v150, v21
	v_max_i32_e32 v156, v158, v159
	v_min_i32_e32 v159, v158, v159
	v_max_i32_e32 v20, v160, v161
	v_min_i32_e32 v161, v160, v161
	v_max_i32_e32 v155, v156, v20
	v_min_i32_e32 v20, v156, v20
	v_max_i32_e32 v150, v159, v161
	v_min_i32_e32 v161, v159, v161
	v_max_i32_e32 v158, v150, v20
	v_min_i32_e32 v20, v150, v20
	v_max_i32_e32 v160, v19, v155
	v_min_i32_e32 v155, v19, v155
	v_max_i32_e32 v156, v21, v20
	v_min_i32_e32 v20, v21, v20
	v_max_i32_e32 v159, v156, v155
	v_min_i32_e32 v155, v156, v155
	v_max_i32_e32 v150, v154, v158
	v_min_i32_e32 v158, v154, v158
	v_max_i32_e32 v19, v157, v161
	v_min_i32_e32 v161, v157, v161
	v_max_i32_e32 v21, v19, v158
	v_min_i32_e32 v158, v19, v158
	v_max_i32_e32 v156, v150, v159
	v_min_i32_e32 v159, v150, v159
	v_max_i32_e32 v154, v21, v155
	v_min_i32_e32 v155, v21, v155
	v_max_i32_e32 v157, v158, v20
	v_min_i32_e32 v20, v158, v20
	v_max_i32_e32 v19, v152, v160
	v_min_i32_e32 v160, v152, v160
	v_max_i32_e32 v150, v147, v155
	v_min_i32_e32 v155, v147, v155
	v_max_i32_e32 v21, v150, v160
	v_min_i32_e32 v160, v150, v160
	v_max_i32_e32 v158, v151, v159
	v_min_i32_e32 v159, v151, v159
	v_max_i32_e32 v152, v18, v20
	v_min_i32_e32 v20, v18, v20
	v_max_i32_e32 v147, v152, v159
	v_min_i32_e32 v159, v152, v159
	v_max_i32_e32 v150, v158, v21
	v_min_i32_e32 v21, v158, v21
	v_max_i32_e32 v151, v147, v160
	v_min_i32_e32 v160, v147, v160
	v_max_i32_e32 v18, v159, v155
	v_min_i32_e32 v155, v159, v155
	v_max_i32_e32 v152, v148, v156
	v_min_i32_e32 v156, v148, v156
	v_max_i32_e32 v158, v149, v157
	v_min_i32_e32 v157, v149, v157
	v_max_i32_e32 v147, v158, v156
	v_min_i32_e32 v156, v158, v156
	v_max_i32_e32 v159, v146, v154
	v_min_i32_e32 v154, v146, v154
	v_max_i32_e32 v148, v153, v161
	v_min_i32_e32 v161, v153, v161
	v_max_i32_e32 v149, v148, v154
	v_min_i32_e32 v154, v148, v154
	v_max_i32_e32 v158, v159, v147
	v_min_i32_e32 v147, v159, v147
	v_max_i32_e32 v146, v149, v156
	v_min_i32_e32 v156, v149, v156
	v_max_i32_e32 v153, v154, v157
	v_min_i32_e32 v157, v154, v157
	v_max_i32_e32 v148, v152, v150
	v_min_i32_e32 v150, v152, v150
	v_max_i32_e32 v159, v158, v21
	v_min_i32_e32 v21, v158, v21
	v_max_i32_e32 v149, v147, v151
	v_min_i32_e32 v151, v147, v151
	v_max_i32_e32 v154, v146, v160
	v_min_i32_e32 v160, v146, v160
	v_max_i32_e32 v152, v156, v18
	v_min_i32_e32 v18, v156, v18
	v_max_i32_e32 v158, v153, v155
	v_min_i32_e32 v155, v153, v155
	v_max_i32_e32 v147, v157, v20
	v_min_i32_e32 v20, v157, v20
; #define LAS __attribute__((address_space(3)))
; #define TOPK_INSERT(arr, xx) do { int _x = (xx); _Pragma("unroll") for (int _j = 0; _j < 16; ++_j) { const int _hi = max(arr[_j], _x); _x = min(arr[_j], _x); arr[_j] = _hi; } } while (0)
; DI void routing_block(LAS unsigned char* lds, const bf16* q, const bf16* skb, int* experts, float* pgates, int tb) {
;     ...
;             int a[16];
; #pragma unroll
;             for (int j = 0; j < 16; ++j) a[j] = (int)0x80000000;
;             LAS int* row = sc + (tid >> 1) * RT_PITCH; const int hf = tid & 1;
; #pragma unroll 8
;             for (int k = 0; k < 64; ++k) { const int x = row[64 * hf + k]; TOPK_INSERT(a, x); }
	v_max_i32_e32 v146, v162, v163
	v_min_i32_e32 v163, v162, v163
	v_max_i32_e32 v156, v164, v165
	v_min_i32_e32 v165, v164, v165
	v_max_i32_e32 v153, v146, v156
	v_min_i32_e32 v156, v146, v156
	v_max_i32_e32 v157, v163, v165
	v_min_i32_e32 v165, v163, v165
	v_max_i32_e32 v162, v157, v156
	v_min_i32_e32 v156, v157, v156
	v_max_i32_e32 v164, v166, v167
	v_min_i32_e32 v167, v166, v167
	v_max_i32_e32 v146, v168, v169
	v_min_i32_e32 v169, v168, v169
	v_max_i32_e32 v163, v164, v146
	v_min_i32_e32 v146, v164, v146
	v_max_i32_e32 v157, v167, v169
	v_min_i32_e32 v169, v167, v169
	v_max_i32_e32 v166, v157, v146
	v_min_i32_e32 v146, v157, v146
	v_max_i32_e32 v168, v153, v163
	v_min_i32_e32 v163, v153, v163
	v_max_i32_e32 v164, v156, v146
	v_min_i32_e32 v146, v156, v146
	v_max_i32_e32 v167, v164, v163
	v_min_i32_e32 v163, v164, v163
	v_max_i32_e32 v157, v162, v166
	v_min_i32_e32 v166, v162, v166
	v_max_i32_e32 v153, v165, v169
	v_min_i32_e32 v169, v165, v169
	v_max_i32_e32 v156, v153, v166
	v_min_i32_e32 v166, v153, v166
	v_max_i32_e32 v164, v157, v167
	v_min_i32_e32 v167, v157, v167
	v_max_i32_e32 v162, v156, v163
	v_min_i32_e32 v163, v156, v163
	v_max_i32_e32 v165, v166, v146
	v_min_i32_e32 v146, v166, v146
	v_max_i32_e32 v153, v170, v171
	v_min_i32_e32 v171, v170, v171
	v_max_i32_e32 v157, v172, v173
	v_min_i32_e32 v173, v172, v173
	v_max_i32_e32 v156, v153, v157
	v_min_i32_e32 v157, v153, v157
	v_max_i32_e32 v166, v171, v173
	v_min_i32_e32 v173, v171, v173
	v_max_i32_e32 v170, v166, v157
	v_min_i32_e32 v157, v166, v157
	v_max_i32_e32 v172, v174, v175
	v_min_i32_e32 v175, v174, v175
	v_max_i32_e32 v153, v176, v177
	v_min_i32_e32 v177, v176, v177
	v_max_i32_e32 v171, v172, v153
	v_min_i32_e32 v153, v172, v153
	v_max_i32_e32 v166, v175, v177
	v_min_i32_e32 v177, v175, v177
	v_max_i32_e32 v174, v166, v153
	v_min_i32_e32 v153, v166, v153
	v_max_i32_e32 v176, v156, v171
	v_min_i32_e32 v171, v156, v171
	v_max_i32_e32 v172, v157, v153
	v_min_i32_e32 v153, v157, v153
	v_max_i32_e32 v175, v172, v171
	v_min_i32_e32 v171, v172, v171
	v_max_i32_e32 v166, v170, v174
	v_min_i32_e32 v174, v170, v174
	v_max_i32_e32 v156, v173, v177
	v_min_i32_e32 v177, v173, v177
	v_max_i32_e32 v157, v156, v174
	v_min_i32_e32 v174, v156, v174
	v_max_i32_e32 v172, v166, v175
	v_min_i32_e32 v175, v166, v175
	v_max_i32_e32 v170, v157, v171
	v_min_i32_e32 v171, v157, v171
	v_max_i32_e32 v173, v174, v153
	v_min_i32_e32 v153, v174, v153
	v_max_i32_e32 v156, v168, v176
	v_min_i32_e32 v176, v168, v176
	v_max_i32_e32 v166, v163, v171
	v_min_i32_e32 v171, v163, v171
	v_max_i32_e32 v157, v166, v176
	v_min_i32_e32 v176, v166, v176
	v_max_i32_e32 v174, v167, v175
	v_min_i32_e32 v175, v167, v175
	v_max_i32_e32 v168, v146, v153
	v_min_i32_e32 v153, v146, v153
	v_max_i32_e32 v163, v168, v175
	v_min_i32_e32 v175, v168, v175
	v_max_i32_e32 v166, v174, v157
	v_min_i32_e32 v157, v174, v157
	v_max_i32_e32 v167, v163, v176
	v_min_i32_e32 v176, v163, v176
	v_max_i32_e32 v146, v175, v171
	v_min_i32_e32 v171, v175, v171
	v_max_i32_e32 v168, v164, v172
	v_min_i32_e32 v172, v164, v172
	v_max_i32_e32 v174, v165, v173
	v_min_i32_e32 v173, v165, v173
	v_max_i32_e32 v163, v174, v172
	v_min_i32_e32 v172, v174, v172
	v_max_i32_e32 v175, v162, v170
	v_min_i32_e32 v170, v162, v170
	v_max_i32_e32 v164, v169, v177
	v_min_i32_e32 v177, v169, v177
	v_max_i32_e32 v165, v164, v170
	v_min_i32_e32 v170, v164, v170
	v_max_i32_e32 v174, v175, v163
	v_min_i32_e32 v163, v175, v163
	v_max_i32_e32 v162, v165, v172
	v_min_i32_e32 v172, v165, v172
	v_max_i32_e32 v169, v170, v173
	v_min_i32_e32 v173, v170, v173
	v_max_i32_e32 v164, v168, v166
	v_min_i32_e32 v166, v168, v166
	v_max_i32_e32 v175, v174, v157
	v_min_i32_e32 v157, v174, v157
	v_max_i32_e32 v165, v163, v167
	v_min_i32_e32 v167, v163, v167
	v_max_i32_e32 v170, v162, v176
	v_min_i32_e32 v176, v162, v176
	v_max_i32_e32 v168, v172, v146
	v_min_i32_e32 v146, v172, v146
	v_max_i32_e32 v174, v169, v171
	v_min_i32_e32 v171, v169, v171
	v_max_i32_e32 v163, v173, v153
	v_min_i32_e32 v153, v173, v153
	v_max_i32_e32 v162, v178, v179
	v_min_i32_e32 v179, v178, v179
	v_max_i32_e32 v172, v180, v181
	v_min_i32_e32 v181, v180, v181
	v_max_i32_e32 v169, v162, v172
	v_min_i32_e32 v172, v162, v172
	v_max_i32_e32 v173, v179, v181
	v_min_i32_e32 v181, v179, v181
	v_max_i32_e32 v178, v173, v172
	v_min_i32_e32 v172, v173, v172
	v_max_i32_e32 v180, v182, v183
	v_min_i32_e32 v183, v182, v183
	v_max_i32_e32 v162, v184, v185
	v_min_i32_e32 v185, v184, v185
	v_max_i32_e32 v179, v180, v162
	v_min_i32_e32 v162, v180, v162
	v_max_i32_e32 v173, v183, v185
	v_min_i32_e32 v185, v183, v185
	v_max_i32_e32 v182, v173, v162
	v_min_i32_e32 v162, v173, v162
	v_max_i32_e32 v184, v169, v179
	v_min_i32_e32 v179, v169, v179
	v_max_i32_e32 v180, v172, v162
	v_min_i32_e32 v162, v172, v162
	v_max_i32_e32 v183, v180, v179
	v_min_i32_e32 v179, v180, v179
	v_max_i32_e32 v173, v178, v182
	v_min_i32_e32 v182, v178, v182
	v_max_i32_e32 v169, v181, v185
	v_min_i32_e32 v185, v181, v185
	v_max_i32_e32 v172, v169, v182
	v_min_i32_e32 v182, v169, v182
	v_max_i32_e32 v180, v173, v183
	v_min_i32_e32 v183, v173, v183
	v_max_i32_e32 v178, v172, v179
	v_min_i32_e32 v179, v172, v179
	v_max_i32_e32 v181, v182, v162
	v_min_i32_e32 v162, v182, v162
	v_max_i32_e32 v169, v186, v187
	v_min_i32_e32 v187, v186, v187
	v_max_i32_e32 v173, v188, v189
	v_min_i32_e32 v189, v188, v189
	v_max_i32_e32 v172, v169, v173
	v_min_i32_e32 v173, v169, v173
	v_max_i32_e32 v182, v187, v189
	v_min_i32_e32 v189, v187, v189
	v_max_i32_e32 v186, v182, v173
	v_min_i32_e32 v173, v182, v173
	v_max_i32_e32 v188, v190, v191
	v_min_i32_e32 v191, v190, v191
; #define LAS __attribute__((address_space(3)))
; #define TOPK_INSERT(arr, xx) do { int _x = (xx); _Pragma("unroll") for (int _j = 0; _j < 16; ++_j) { const int _hi = max(arr[_j], _x); _x = min(arr[_j], _x); arr[_j] = _hi; } } while (0)
; DI void routing_block(LAS unsigned char* lds, const bf16* q, const bf16* skb, int* experts, float* pgates, int tb) {
;     ...
;             int a[16];
; #pragma unroll
;             for (int j = 0; j < 16; ++j) a[j] = (int)0x80000000;
;             LAS int* row = sc + (tid >> 1) * RT_PITCH; const int hf = tid & 1;
; #pragma unroll 8
;             for (int k = 0; k < 64; ++k) { const int x = row[64 * hf + k]; TOPK_INSERT(a, x); }
	v_max_i32_e32 v169, v192, v193
	v_min_i32_e32 v193, v192, v193
	v_max_i32_e32 v187, v188, v169
	v_min_i32_e32 v169, v188, v169
	v_max_i32_e32 v182, v191, v193
	v_min_i32_e32 v193, v191, v193
	v_max_i32_e32 v190, v182, v169
	v_min_i32_e32 v169, v182, v169
	v_max_i32_e32 v192, v172, v187
	v_min_i32_e32 v187, v172, v187
	v_max_i32_e32 v188, v173, v169
	v_min_i32_e32 v169, v173, v169
	v_max_i32_e32 v191, v188, v187
	v_min_i32_e32 v187, v188, v187
	v_max_i32_e32 v182, v186, v190
	v_min_i32_e32 v190, v186, v190
	v_max_i32_e32 v172, v189, v193
	v_min_i32_e32 v193, v189, v193
	v_max_i32_e32 v173, v172, v190
	v_min_i32_e32 v190, v172, v190
	v_max_i32_e32 v188, v182, v191
	v_min_i32_e32 v191, v182, v191
	v_max_i32_e32 v186, v173, v187
	v_min_i32_e32 v187, v173, v187
	v_max_i32_e32 v189, v190, v169
	v_min_i32_e32 v169, v190, v169
	v_max_i32_e32 v172, v184, v192
	v_min_i32_e32 v192, v184, v192
	v_max_i32_e32 v182, v179, v187
	v_min_i32_e32 v187, v179, v187
	v_max_i32_e32 v173, v182, v192
	v_min_i32_e32 v192, v182, v192
	v_max_i32_e32 v190, v183, v191
	v_min_i32_e32 v191, v183, v191
	v_max_i32_e32 v184, v162, v169
	v_min_i32_e32 v169, v162, v169
	v_max_i32_e32 v179, v184, v191
	v_min_i32_e32 v191, v184, v191
	v_max_i32_e32 v182, v190, v173
	v_min_i32_e32 v173, v190, v173
	v_max_i32_e32 v183, v179, v192
	v_min_i32_e32 v192, v179, v192
	v_max_i32_e32 v162, v191, v187
	v_min_i32_e32 v187, v191, v187
	v_max_i32_e32 v184, v180, v188
	v_min_i32_e32 v188, v180, v188
	v_max_i32_e32 v190, v181, v189
	v_min_i32_e32 v189, v181, v189
	v_max_i32_e32 v179, v190, v188
	v_min_i32_e32 v188, v190, v188
	v_max_i32_e32 v191, v178, v186
	v_min_i32_e32 v186, v178, v186
	v_max_i32_e32 v180, v185, v193
	v_min_i32_e32 v193, v185, v193
	v_max_i32_e32 v181, v180, v186
	v_min_i32_e32 v186, v180, v186
	v_max_i32_e32 v190, v191, v179
	v_min_i32_e32 v179, v191, v179
	v_max_i32_e32 v178, v181, v188
	v_min_i32_e32 v188, v181, v188
	v_max_i32_e32 v185, v186, v189
	v_min_i32_e32 v189, v186, v189
	v_max_i32_e32 v180, v184, v182
	v_min_i32_e32 v182, v184, v182
	v_max_i32_e32 v191, v190, v173
	v_min_i32_e32 v173, v190, v173
	v_max_i32_e32 v181, v179, v183
	v_min_i32_e32 v183, v179, v183
	v_max_i32_e32 v186, v178, v192
	v_min_i32_e32 v192, v178, v192
	v_max_i32_e32 v184, v188, v162
	v_min_i32_e32 v162, v188, v162
	v_max_i32_e32 v190, v185, v187
	v_min_i32_e32 v187, v185, v187
	v_max_i32_e32 v179, v189, v169
	v_min_i32_e32 v169, v189, v169
	v_max_i32_e32 v178, v194, v195
	v_min_i32_e32 v195, v194, v195
	v_max_i32_e32 v188, v196, v197
	v_min_i32_e32 v197, v196, v197
	v_max_i32_e32 v185, v178, v188
	v_min_i32_e32 v188, v178, v188
	v_max_i32_e32 v189, v195, v197
	v_min_i32_e32 v197, v195, v197
	v_max_i32_e32 v194, v189, v188
	v_min_i32_e32 v188, v189, v188
	v_max_i32_e32 v196, v198, v199
	v_min_i32_e32 v199, v198, v199
	v_max_i32_e32 v178, v200, v201
	v_min_i32_e32 v201, v200, v201
	v_max_i32_e32 v195, v196, v178
	v_min_i32_e32 v178, v196, v178
	v_max_i32_e32 v189, v199, v201
	v_min_i32_e32 v201, v199, v201
	v_max_i32_e32 v198, v189, v178
	v_min_i32_e32 v178, v189, v178
	v_max_i32_e32 v200, v185, v195
	v_min_i32_e32 v195, v185, v195
	v_max_i32_e32 v196, v188, v178
	v_min_i32_e32 v178, v188, v178
	v_max_i32_e32 v199, v196, v195
	v_min_i32_e32 v195, v196, v195
	v_max_i32_e32 v189, v194, v198
	v_min_i32_e32 v198, v194, v198
	v_max_i32_e32 v185, v197, v201
	v_min_i32_e32 v201, v197, v201
	v_max_i32_e32 v188, v185, v198
	v_min_i32_e32 v198, v185, v198
	v_max_i32_e32 v196, v189, v199
	v_min_i32_e32 v199, v189, v199
	v_max_i32_e32 v194, v188, v195
	v_min_i32_e32 v195, v188, v195
	v_max_i32_e32 v197, v198, v178
	v_min_i32_e32 v178, v198, v178
	v_max_i32_e32 v185, v202, v203
	v_min_i32_e32 v203, v202, v203
	v_max_i32_e32 v189, v204, v205
	v_min_i32_e32 v205, v204, v205
	v_max_i32_e32 v188, v185, v189
	v_min_i32_e32 v189, v185, v189
	v_max_i32_e32 v198, v203, v205
	v_min_i32_e32 v205, v203, v205
	v_max_i32_e32 v202, v198, v189
	v_min_i32_e32 v189, v198, v189
	v_max_i32_e32 v204, v206, v207
	v_min_i32_e32 v207, v206, v207
	v_max_i32_e32 v185, v208, v209
	v_min_i32_e32 v209, v208, v209
	v_max_i32_e32 v203, v204, v185
	v_min_i32_e32 v185, v204, v185
	v_max_i32_e32 v198, v207, v209
	v_min_i32_e32 v209, v207, v209
	v_max_i32_e32 v206, v198, v185
	v_min_i32_e32 v185, v198, v185
	v_max_i32_e32 v208, v188, v203
	v_min_i32_e32 v203, v188, v203
	v_max_i32_e32 v204, v189, v185
	v_min_i32_e32 v185, v189, v185
	v_max_i32_e32 v207, v204, v203
	v_min_i32_e32 v203, v204, v203
	v_max_i32_e32 v198, v202, v206
	v_min_i32_e32 v206, v202, v206
	v_max_i32_e32 v188, v205, v209
	v_min_i32_e32 v209, v205, v209
	v_max_i32_e32 v189, v188, v206
	v_min_i32_e32 v206, v188, v206
	v_max_i32_e32 v204, v198, v207
	v_min_i32_e32 v207, v198, v207
	v_max_i32_e32 v202, v189, v203
	v_min_i32_e32 v203, v189, v203
	v_max_i32_e32 v205, v206, v185
	v_min_i32_e32 v185, v206, v185
	v_max_i32_e32 v188, v200, v208
	v_min_i32_e32 v208, v200, v208
	v_max_i32_e32 v198, v195, v203
	v_min_i32_e32 v203, v195, v203
	v_max_i32_e32 v189, v198, v208
	v_min_i32_e32 v208, v198, v208
	v_max_i32_e32 v206, v199, v207
	v_min_i32_e32 v207, v199, v207
	v_max_i32_e32 v200, v178, v185
	v_min_i32_e32 v185, v178, v185
	v_max_i32_e32 v195, v200, v207
	v_min_i32_e32 v207, v200, v207
	v_max_i32_e32 v198, v206, v189
	v_min_i32_e32 v189, v206, v189
	v_max_i32_e32 v199, v195, v208
	v_min_i32_e32 v208, v195, v208
	v_max_i32_e32 v178, v207, v203
	v_min_i32_e32 v203, v207, v203
	v_max_i32_e32 v200, v196, v204
	v_min_i32_e32 v204, v196, v204
	v_max_i32_e32 v206, v197, v205
	v_min_i32_e32 v205, v197, v205
	v_max_i32_e32 v195, v206, v204
	v_min_i32_e32 v204, v206, v204
; #define LAS __attribute__((address_space(3)))
; #define TOPK_INSERT(arr, xx) do { int _x = (xx); _Pragma("unroll") for (int _j = 0; _j < 16; ++_j) { const int _hi = max(arr[_j], _x); _x = min(arr[_j], _x); arr[_j] = _hi; } } while (0)
; DI void routing_block(LAS unsigned char* lds, const bf16* q, const bf16* skb, int* experts, float* pgates, int tb) {
;     ...
;             int a[16];
; #pragma unroll
;             for (int j = 0; j < 16; ++j) a[j] = (int)0x80000000;
;             LAS int* row = sc + (tid >> 1) * RT_PITCH; const int hf = tid & 1;
; #pragma unroll 8
;             for (int k = 0; k < 64; ++k) { const int x = row[64 * hf + k]; TOPK_INSERT(a, x); }
;             __syncthreads();
; #pragma unroll
;             for (int j = 0; j < 16; ++j) row[16 * hf + j] = a[j];
;             __syncthreads();
;             if (hf == 0) {
; #pragma unroll
;                 for (int j = 0; j < 16; ++j) { const int x = row[16 + j]; TOPK_INSERT(a, x); }
; #pragma unroll
;                 for (int j = 0; j < 16; ++j) row[j] = a[j];
	v_max_i32_e32 v207, v194, v202
	v_min_i32_e32 v202, v194, v202
	v_max_i32_e32 v196, v201, v209
	v_min_i32_e32 v209, v201, v209
	v_max_i32_e32 v197, v196, v202
	v_min_i32_e32 v202, v196, v202
	v_max_i32_e32 v206, v207, v195
	v_min_i32_e32 v195, v207, v195
	v_max_i32_e32 v194, v197, v204
	v_min_i32_e32 v204, v197, v204
	v_max_i32_e32 v201, v202, v205
	v_min_i32_e32 v205, v202, v205
	v_max_i32_e32 v196, v200, v198
	v_min_i32_e32 v198, v200, v198
	v_max_i32_e32 v207, v206, v189
	v_min_i32_e32 v189, v206, v189
	v_max_i32_e32 v197, v195, v199
	v_min_i32_e32 v199, v195, v199
	v_max_i32_e32 v202, v194, v208
	v_min_i32_e32 v208, v194, v208
	v_max_i32_e32 v200, v204, v178
	v_min_i32_e32 v178, v204, v178
	v_max_i32_e32 v206, v201, v203
	v_min_i32_e32 v203, v201, v203
	v_max_i32_e32 v195, v205, v185
	v_min_i32_e32 v185, v205, v185
	v_max_i32_e32 v19, v19, v177
	v_max_i32_e32 v148, v148, v153
	v_max_i32_e32 v150, v150, v163
	v_max_i32_e32 v159, v159, v171
	v_max_i32_e32 v21, v21, v174
	v_max_i32_e32 v149, v149, v146
	v_max_i32_e32 v151, v151, v168
	v_max_i32_e32 v154, v154, v176
	v_max_i32_e32 v160, v160, v170
	v_max_i32_e32 v152, v152, v167
	v_max_i32_e32 v18, v18, v165
	v_max_i32_e32 v158, v158, v157
	v_max_i32_e32 v155, v155, v175
	v_max_i32_e32 v147, v147, v166
	v_max_i32_e32 v20, v20, v164
	v_max_i32_e32 v161, v161, v156
	v_max_i32_e32 v194, v19, v160
	v_min_i32_e32 v160, v19, v160
	v_max_i32_e32 v204, v148, v152
	v_min_i32_e32 v152, v148, v152
	v_max_i32_e32 v201, v150, v18
	v_min_i32_e32 v18, v150, v18
	v_max_i32_e32 v205, v159, v158
	v_min_i32_e32 v158, v159, v158
	v_max_i32_e32 v156, v21, v155
	v_min_i32_e32 v155, v21, v155
	v_max_i32_e32 v164, v149, v147
	v_min_i32_e32 v147, v149, v147
	v_max_i32_e32 v166, v151, v20
	v_min_i32_e32 v20, v151, v20
	v_max_i32_e32 v175, v154, v161
	v_min_i32_e32 v161, v154, v161
	v_max_i32_e32 v157, v194, v156
	v_min_i32_e32 v156, v194, v156
	v_max_i32_e32 v165, v204, v164
	v_min_i32_e32 v164, v204, v164
	v_max_i32_e32 v167, v201, v166
	v_min_i32_e32 v166, v201, v166
	v_max_i32_e32 v170, v205, v175
	v_min_i32_e32 v175, v205, v175
	v_max_i32_e32 v176, v160, v155
	v_min_i32_e32 v155, v160, v155
	v_max_i32_e32 v168, v152, v147
	v_min_i32_e32 v147, v152, v147
	v_max_i32_e32 v146, v18, v20
	v_min_i32_e32 v20, v18, v20
	v_max_i32_e32 v174, v158, v161
	v_min_i32_e32 v161, v158, v161
	v_max_i32_e32 v171, v157, v167
	v_min_i32_e32 v167, v157, v167
	v_max_i32_e32 v163, v165, v170
	v_min_i32_e32 v170, v165, v170
	v_max_i32_e32 v153, v156, v166
	v_min_i32_e32 v166, v156, v166
	v_max_i32_e32 v177, v164, v175
	v_min_i32_e32 v175, v164, v175
	v_max_i32_e32 v19, v176, v146
	v_min_i32_e32 v146, v176, v146
	v_max_i32_e32 v148, v168, v174
	v_min_i32_e32 v174, v168, v174
	v_max_i32_e32 v150, v155, v20
	v_min_i32_e32 v20, v155, v20
	v_max_i32_e32 v159, v147, v161
	v_min_i32_e32 v161, v147, v161
	v_max_i32_e32 v21, v171, v163
	v_min_i32_e32 v163, v171, v163
	v_max_i32_e32 v149, v167, v170
	v_min_i32_e32 v170, v167, v170
	v_max_i32_e32 v151, v153, v177
	v_min_i32_e32 v177, v153, v177
	v_max_i32_e32 v154, v166, v175
	v_min_i32_e32 v175, v166, v175
	v_max_i32_e32 v194, v19, v148
	v_min_i32_e32 v148, v19, v148
	v_max_i32_e32 v204, v146, v174
	v_min_i32_e32 v174, v146, v174
	v_max_i32_e32 v201, v150, v159
	v_min_i32_e32 v159, v150, v159
	v_max_i32_e32 v205, v20, v161
	v_min_i32_e32 v161, v20, v161
	v_max_i32_e32 v172, v172, v209
	v_max_i32_e32 v180, v180, v185
	v_max_i32_e32 v182, v182, v195
	v_max_i32_e32 v191, v191, v203
	v_max_i32_e32 v173, v173, v206
	v_max_i32_e32 v181, v181, v178
	v_max_i32_e32 v183, v183, v200
	v_max_i32_e32 v186, v186, v208
	v_max_i32_e32 v192, v192, v202
	v_max_i32_e32 v184, v184, v199
	v_max_i32_e32 v162, v162, v197
	v_max_i32_e32 v190, v190, v189
	v_max_i32_e32 v187, v187, v207
	v_max_i32_e32 v179, v179, v198
	v_max_i32_e32 v169, v169, v196
	v_max_i32_e32 v193, v193, v188
	v_max_i32_e32 v160, v172, v192
	v_min_i32_e32 v192, v172, v192
	v_max_i32_e32 v152, v180, v184
	v_min_i32_e32 v184, v180, v184
	v_max_i32_e32 v18, v182, v162
	v_min_i32_e32 v162, v182, v162
	v_max_i32_e32 v158, v191, v190
	v_min_i32_e32 v190, v191, v190
	v_max_i32_e32 v157, v173, v187
	v_min_i32_e32 v187, v173, v187
	v_max_i32_e32 v165, v181, v179
	v_min_i32_e32 v179, v181, v179
	v_max_i32_e32 v156, v183, v169
	v_min_i32_e32 v169, v183, v169
	v_max_i32_e32 v164, v186, v193
	v_min_i32_e32 v193, v186, v193
	v_max_i32_e32 v176, v160, v157
	v_min_i32_e32 v157, v160, v157
	v_max_i32_e32 v168, v152, v165
	v_min_i32_e32 v165, v152, v165
	v_max_i32_e32 v155, v18, v156
	v_min_i32_e32 v156, v18, v156
	v_max_i32_e32 v147, v158, v164
	v_min_i32_e32 v164, v158, v164
	v_max_i32_e32 v171, v192, v187
	v_min_i32_e32 v187, v192, v187
	v_max_i32_e32 v167, v184, v179
	v_min_i32_e32 v179, v184, v179
	v_max_i32_e32 v153, v162, v169
	v_min_i32_e32 v169, v162, v169
	v_max_i32_e32 v166, v190, v193
	v_min_i32_e32 v193, v190, v193
	v_max_i32_e32 v19, v176, v155
	v_min_i32_e32 v155, v176, v155
	v_max_i32_e32 v146, v168, v147
	v_min_i32_e32 v147, v168, v147
	v_max_i32_e32 v150, v157, v156
	v_min_i32_e32 v156, v157, v156
	v_max_i32_e32 v20, v165, v164
	v_min_i32_e32 v164, v165, v164
	v_max_i32_e32 v188, v171, v153
	v_min_i32_e32 v153, v171, v153
	v_max_i32_e32 v196, v167, v166
	v_min_i32_e32 v166, v167, v166
	v_max_i32_e32 v198, v187, v169
	v_min_i32_e32 v169, v187, v169
	v_max_i32_e32 v207, v179, v193
	v_min_i32_e32 v193, v179, v193
	v_max_i32_e32 v189, v19, v146
	v_min_i32_e32 v146, v19, v146
	v_max_i32_e32 v197, v155, v147
	v_min_i32_e32 v147, v155, v147
	v_max_i32_e32 v199, v150, v20
	v_min_i32_e32 v20, v150, v20
	v_max_i32_e32 v202, v156, v164
	v_min_i32_e32 v164, v156, v164
; #define TOPK_INSERT(arr, xx) do { int _x = (xx); _Pragma("unroll") for (int _j = 0; _j < 16; ++_j) { const int _hi = max(arr[_j], _x); _x = min(arr[_j], _x); arr[_j] = _hi; } } while (0)
; DI void routing_block(LAS unsigned char* lds, const bf16* q, const bf16* skb, int* experts, float* pgates, int tb) {
;     ...
;             __syncthreads();
; #pragma unroll
;             for (int j = 0; j < 16; ++j) row[16 * hf + j] = a[j];
;             __syncthreads();
;             if (hf == 0) {
; #pragma unroll
;                 for (int j = 0; j < 16; ++j) { const int x = row[16 + j]; TOPK_INSERT(a, x); }
; #pragma unroll
;                 for (int j = 0; j < 16; ++j) row[j] = a[j];
;             }
	v_max_i32_e32 v208, v188, v196
	v_min_i32_e32 v196, v188, v196
	v_max_i32_e32 v200, v153, v166
	v_min_i32_e32 v166, v153, v166
	v_max_i32_e32 v178, v198, v207
	v_min_i32_e32 v207, v198, v207
	v_max_i32_e32 v206, v169, v193
	v_min_i32_e32 v193, v169, v193
	v_max_i32_e32 v21, v21, v193
	v_max_i32_e32 v163, v163, v206
	v_max_i32_e32 v149, v149, v207
	v_max_i32_e32 v170, v170, v178
	v_max_i32_e32 v151, v151, v166
	v_max_i32_e32 v177, v177, v200
	v_max_i32_e32 v154, v154, v196
	v_max_i32_e32 v175, v175, v208
	v_max_i32_e32 v194, v194, v164
	v_max_i32_e32 v148, v148, v202
	v_max_i32_e32 v204, v204, v20
	v_max_i32_e32 v174, v174, v199
	v_max_i32_e32 v201, v201, v147
	v_max_i32_e32 v159, v159, v197
	v_max_i32_e32 v205, v205, v146
	v_max_i32_e32 v161, v161, v189
	v_max_i32_e32 v203, v21, v194
	v_min_i32_e32 v194, v21, v194
	v_max_i32_e32 v195, v163, v148
	v_min_i32_e32 v148, v163, v148
	v_max_i32_e32 v185, v149, v204
	v_min_i32_e32 v204, v149, v204
	v_max_i32_e32 v209, v170, v174
	v_min_i32_e32 v174, v170, v174
	v_max_i32_e32 v172, v151, v201
	v_min_i32_e32 v201, v151, v201
	v_max_i32_e32 v180, v177, v159
	v_min_i32_e32 v159, v177, v159
	v_max_i32_e32 v182, v154, v205
	v_min_i32_e32 v205, v154, v205
	v_max_i32_e32 v191, v175, v161
	v_min_i32_e32 v161, v175, v161
	v_max_i32_e32 v173, v203, v172
	v_min_i32_e32 v172, v203, v172
	v_max_i32_e32 v181, v195, v180
	v_min_i32_e32 v180, v195, v180
	v_max_i32_e32 v183, v185, v182
	v_min_i32_e32 v182, v185, v182
	v_max_i32_e32 v186, v209, v191
	v_min_i32_e32 v191, v209, v191
	v_max_i32_e32 v160, v194, v201
	v_min_i32_e32 v201, v194, v201
	v_max_i32_e32 v152, v148, v159
	v_min_i32_e32 v159, v148, v159
	v_max_i32_e32 v18, v204, v205
	v_min_i32_e32 v205, v204, v205
	v_max_i32_e32 v158, v174, v161
	v_min_i32_e32 v161, v174, v161
	v_max_i32_e32 v192, v173, v183
	v_min_i32_e32 v183, v173, v183
	v_max_i32_e32 v184, v181, v186
	v_min_i32_e32 v186, v181, v186
	v_max_i32_e32 v162, v172, v182
	v_min_i32_e32 v182, v172, v182
	v_max_i32_e32 v190, v180, v191
	v_min_i32_e32 v191, v180, v191
	v_max_i32_e32 v176, v160, v18
	v_min_i32_e32 v18, v160, v18
	v_max_i32_e32 v168, v152, v158
	v_min_i32_e32 v158, v152, v158
	v_max_i32_e32 v157, v201, v205
	v_min_i32_e32 v205, v201, v205
	v_max_i32_e32 v165, v159, v161
	v_min_i32_e32 v161, v159, v161
	v_max_i32_e32 v171, v192, v184
	v_min_i32_e32 v184, v192, v184
	v_max_i32_e32 v167, v183, v186
	v_min_i32_e32 v186, v183, v186
	v_max_i32_e32 v187, v162, v190
	v_min_i32_e32 v190, v162, v190
	v_max_i32_e32 v179, v182, v191
	v_min_i32_e32 v191, v182, v191
	v_max_i32_e32 v19, v176, v168
	v_min_i32_e32 v168, v176, v168
	v_max_i32_e32 v155, v18, v158
	v_min_i32_e32 v158, v18, v158
	v_max_i32_e32 v150, v157, v165
	v_min_i32_e32 v165, v157, v165
	v_max_i32_e32 v156, v205, v161
	v_min_i32_e32 v161, v205, v161
	s_barrier
	ds_write2_b32 v136, v171, v184 offset0:0 offset1:1
	ds_write2_b32 v136, v167, v186 offset0:2 offset1:3
	ds_write2_b32 v136, v187, v190 offset0:4 offset1:5
	ds_write2_b32 v136, v179, v191 offset0:6 offset1:7
	ds_write2_b32 v136, v19, v168 offset0:8 offset1:9
	ds_write2_b32 v136, v155, v158 offset0:10 offset1:11
	ds_write2_b32 v136, v150, v165 offset0:12 offset1:13
	ds_write2_b32 v136, v156, v161 offset0:14 offset1:15
	s_waitcnt lgkmcnt(0)
	s_barrier
	s_and_saveexec_b64 s[76:77], s[44:45]
	s_cbranch_execz .LBB0_898
	ds_read2_b32 v[34:35], v119 offset0:16 offset1:17
	ds_read2_b32 v[36:37], v119 offset0:18 offset1:19
	ds_read2_b32 v[38:39], v119 offset0:20 offset1:21
	ds_read2_b32 v[40:41], v119 offset0:22 offset1:23
	ds_read2_b32 v[42:43], v119 offset0:24 offset1:25
	ds_read2_b32 v[44:45], v119 offset0:26 offset1:27
	ds_read2_b32 v[46:47], v119 offset0:28 offset1:29
	ds_read2_b32 v[48:49], v119 offset0:30 offset1:31
	s_waitcnt lgkmcnt(0)
	v_max_i32_e32 v171, v171, v49
	v_max_i32_e32 v184, v184, v48
	v_max_i32_e32 v167, v167, v47
	v_max_i32_e32 v186, v186, v46
	v_max_i32_e32 v187, v187, v45
	v_max_i32_e32 v190, v190, v44
	v_max_i32_e32 v179, v179, v43
	v_max_i32_e32 v191, v191, v42
	v_max_i32_e32 v19, v19, v41
	v_max_i32_e32 v168, v168, v40
	v_max_i32_e32 v155, v155, v39
	v_max_i32_e32 v158, v158, v38
	v_max_i32_e32 v150, v150, v37
	v_max_i32_e32 v165, v165, v36
	v_max_i32_e32 v156, v156, v35
	v_max_i32_e32 v161, v161, v34
	v_max_i32_e32 v188, v171, v19
	v_min_i32_e32 v19, v171, v19
	v_max_i32_e32 v153, v184, v168
	v_min_i32_e32 v168, v184, v168
	v_max_i32_e32 v198, v167, v155
	v_min_i32_e32 v155, v167, v155
	v_max_i32_e32 v169, v186, v158
	v_min_i32_e32 v158, v186, v158
	v_max_i32_e32 v189, v187, v150
	v_min_i32_e32 v150, v187, v150
	v_max_i32_e32 v146, v190, v165
	v_min_i32_e32 v165, v190, v165
	v_max_i32_e32 v197, v179, v156
	v_min_i32_e32 v156, v179, v156
	v_max_i32_e32 v147, v191, v161
	v_min_i32_e32 v161, v191, v161
	v_max_i32_e32 v199, v188, v189
	v_min_i32_e32 v189, v188, v189
	v_max_i32_e32 v20, v153, v146
	v_min_i32_e32 v146, v153, v146
	v_max_i32_e32 v202, v198, v197
	v_min_i32_e32 v197, v198, v197
	v_max_i32_e32 v164, v169, v147
	v_min_i32_e32 v147, v169, v147
	v_max_i32_e32 v208, v19, v150
	v_min_i32_e32 v150, v19, v150
	v_max_i32_e32 v196, v168, v165
	v_min_i32_e32 v165, v168, v165
	v_max_i32_e32 v200, v155, v156
	v_min_i32_e32 v156, v155, v156
	v_max_i32_e32 v166, v158, v161
	v_min_i32_e32 v161, v158, v161
	v_max_i32_e32 v178, v199, v202
	v_min_i32_e32 v202, v199, v202
	v_max_i32_e32 v207, v20, v164
	v_min_i32_e32 v164, v20, v164
	v_max_i32_e32 v206, v189, v197
	v_min_i32_e32 v197, v189, v197
	v_max_i32_e32 v193, v146, v147
	v_min_i32_e32 v147, v146, v147
	v_max_i32_e32 v21, v208, v200
	v_min_i32_e32 v200, v208, v200
	v_max_i32_e32 v163, v196, v166
	v_min_i32_e32 v166, v196, v166
	v_max_i32_e32 v149, v150, v156
	v_min_i32_e32 v156, v150, v156
	v_max_i32_e32 v170, v165, v161
	v_min_i32_e32 v161, v165, v161
	v_max_i32_e32 v151, v178, v207
	v_min_i32_e32 v207, v178, v207
	v_max_i32_e32 v177, v202, v164
	v_min_i32_e32 v164, v202, v164
	v_max_i32_e32 v154, v206, v193
	v_min_i32_e32 v193, v206, v193
	v_max_i32_e32 v175, v197, v147
	v_min_i32_e32 v147, v197, v147
	v_max_i32_e32 v203, v21, v163
	v_min_i32_e32 v163, v21, v163
	v_max_i32_e32 v195, v200, v166
	v_min_i32_e32 v166, v200, v166
	v_max_i32_e32 v185, v149, v170
	v_min_i32_e32 v170, v149, v170
	v_max_i32_e32 v209, v156, v161
	v_min_i32_e32 v161, v156, v161
	ds_write2_b32 v119, v151, v207 offset0:0 offset1:1
	ds_write2_b32 v119, v177, v164 offset0:2 offset1:3
	ds_write2_b32 v119, v154, v193 offset0:4 offset1:5
	ds_write2_b32 v119, v175, v147 offset0:6 offset1:7
	ds_write2_b32 v119, v203, v163 offset0:8 offset1:9
	ds_write2_b32 v119, v195, v166 offset0:10 offset1:11
	ds_write2_b32 v119, v185, v170 offset0:12 offset1:13
	ds_write2_b32 v119, v209, v161 offset0:14 offset1:15
